# v045 with the fused conversion spread over all 16 GEMM1 tile epilogues (6 of 8 waves convert in each, staggered by wave)
# speedup vs baseline: 1.0053x; 1.0053x over previous
.LBB0_1251:
	s_mov_b32 s100, -1
	v_readlane_b32 s23, v255, 55
	s_lshr_b32 s73, s77, 8
	s_cmp_lt_u32 s23, 3
	s_cbranch_scc0 .Lfz_s_skip
	v_lshrrev_b32_e32 v224, 6, v0
	v_readlane_b32 s4, v253, 0
	v_readlane_b32 s5, v253, 1
	v_readfirstlane_b32 s74, v224
	s_add_i32 s73, s73, -1
	s_add_i32 s75, s73, s74
	s_and_b32 s101, s75, 3
	s_cmp_eq_u32 s101, 3
	s_cbranch_scc1 .Lfz_s_skip
	s_lshr_b32 s75, s75, 2
	s_sub_i32 s73, s73, s75
	s_lshr_b32 s75, s74, 2
	s_add_i32 s73, s73, s75
	s_lshl_b32 s73, s73, 11
	s_lshl_b32 s75, s88, 3
	s_add_i32 s73, s73, s75
	s_add_i32 s100, s73, s74
	s_lshr_b32 s73, s100, 9
	s_mul_i32 s74, s73, 0xaaab
	s_lshr_b32 s74, s74, 17
	s_mul_i32 s75, s74, 3
	s_sub_i32 s73, s73, s75
	s_add_i32 s23, s23, 1
	s_lshl_b32 s23, s23, 4
	s_add_i32 s23, s23, s74
	s_lshl_b32 s75, s73, 3
	s_add_i32 s75, s75, 0x80
	s_load_dwordx2 s[4:5], s[4:5], s75
	s_and_b32 s74, s100, 0x1ff
	s_lshr_b32 s75, s74, 5
	s_lshl_b32 s75, s75, 19
	s_and_b32 s101, s74, 31
	s_lshl_b32 s101, s101, 8
	s_or_b32 s75, s75, s101
	s_lshr_b32 s101, s74, 4
	s_lshl_b32 s101, s101, 18
	s_and_b32 s74, s74, 15
	s_lshl_b32 s74, s74, 8
	s_or_b32 s74, s74, s101
	s_cmp_lt_u32 s73, 2
	s_cselect_b32 s75, s75, s74
	s_cselect_b32 s101, 17, 16
	s_mov_b32 s73, 0x1000
	s_cselect_b32 s73, 0x2000, s73
	s_lshl_b32 s74, s23, 23
	s_add_u32 s75, s75, s74
	v_bfe_u32 v224, v0, 4, 2
	v_and_b32_e32 v225, 15, v0
	v_lshlrev_b32_e32 v224, s101, v224
	v_lshl_or_b32 v201, v225, 4, v224
	s_waitcnt lgkmcnt(0)
	s_add_u32 s4, s4, s75
	s_addc_u32 s5, s5, 0
	global_load_dwordx4 v[134:137], v201, s[4:5] nt
	s_add_u32 s4, s4, s73
	s_addc_u32 s5, s5, 0
	global_load_dwordx4 v[138:141], v201, s[4:5] nt
	s_add_u32 s4, s4, s73
	s_addc_u32 s5, s5, 0
	global_load_dwordx4 v[142:145], v201, s[4:5] nt
	s_add_u32 s4, s4, s73
	s_addc_u32 s5, s5, 0
	global_load_dwordx4 v[146:149], v201, s[4:5] nt
	s_add_u32 s4, s4, s73
	s_addc_u32 s5, s5, 0
	global_load_dwordx4 v[150:153], v201, s[4:5] nt
	s_add_u32 s4, s4, s73
	s_addc_u32 s5, s5, 0
	global_load_dwordx4 v[154:157], v201, s[4:5] nt
	s_add_u32 s4, s4, s73
	s_addc_u32 s5, s5, 0
	global_load_dwordx4 v[158:161], v201, s[4:5] nt
	s_add_u32 s4, s4, s73
	s_addc_u32 s5, s5, 0
	global_load_dwordx4 v[162:165], v201, s[4:5] nt
	s_add_u32 s4, s4, s73
	s_addc_u32 s5, s5, 0
	global_load_dwordx4 v[166:169], v201, s[4:5] nt
	s_add_u32 s4, s4, s73
	s_addc_u32 s5, s5, 0
	global_load_dwordx4 v[186:189], v201, s[4:5] nt
	s_add_u32 s4, s4, s73
	s_addc_u32 s5, s5, 0
	global_load_dwordx4 v[190:193], v201, s[4:5] nt
	s_add_u32 s4, s4, s73
	s_addc_u32 s5, s5, 0
	global_load_dwordx4 v[208:211], v201, s[4:5] nt
	s_add_u32 s4, s4, s73
	s_addc_u32 s5, s5, 0
	global_load_dwordx4 v[212:215], v201, s[4:5] nt
	s_add_u32 s4, s4, s73
	s_addc_u32 s5, s5, 0
	global_load_dwordx4 v[216:219], v201, s[4:5] nt
	s_add_u32 s4, s4, s73
	s_addc_u32 s5, s5, 0
	global_load_dwordx4 v[220:223], v201, s[4:5] nt
	s_add_u32 s4, s4, s73
	s_addc_u32 s5, s5, 0
	global_load_dwordx4 v[234:237], v201, s[4:5] nt
